# speedup vs baseline: 1.0072x; 1.0072x over previous
_Z6k_attnPKDv8_DF16_PKfPKhS3_S3_S3_PfS6_S3_S3_PS_S7_:
	v_readfirstlane_b32 s3, v0
	s_cmpk_lt_u32 s2, 0x1a4
	s_mov_b64 s[4:5], -1
	s_cbranch_scc0 .LBB3_37
	s_cmpk_lt_u32 s2, 0x104
	s_cbranch_scc0 .LBB3_27
	s_cmpk_lt_u32 s2, 0x100
	s_cbranch_scc0 .LBB3_20
	s_lshr_b32 s5, s3, 6
	s_lshl_b32 s48, s5, 10
	s_lshl_b32 s3, s2, 1
	s_lshr_b32 s10, s2, 1
	s_bfe_u32 s4, s2, 0x20001
	s_and_b32 s3, s3, 2
	s_bfe_u32 s11, s2, 0x10003
	s_load_dwordx2 s[6:7], s[0:1], 0x0
	s_load_dwordx2 s[8:9], s[0:1], 0x10
	s_load_dwordx2 s[20:21], s[0:1], 0x38
	s_load_dwordx2 s[44:45], s[0:1], 0x8
	s_load_dwordx2 s[46:47], s[0:1], 0x18
	s_or_b32 s3, s3, s11
	s_lshl_b32 s11, s4, 7
	s_and_b32 s10, s10, 0x78
	s_or_b32 s10, s11, s10
	s_add_i32 s5, s10, s5
	s_lshl_b32 s10, s3, 17
	s_lshl_b32 s11, s4, 19
	s_or_b32 s10, s10, s11
	s_waitcnt lgkmcnt(0)
	s_add_u32 s8, s8, s10
	v_mov_b32_e32 v18, 0
	s_addc_u32 s9, s9, 0
	s_mov_b64 s[62:63], s[8:9]
	s_add_u32 s50, s8, 0x8000
	s_addc_u32 s51, s9, 0
	s_add_u32 s52, s8, 0x10000
	s_addc_u32 s53, s9, 0
	v_and_b32_e32 v1, 63, v0
	s_mul_i32 s28, s5, 0xc0
	v_or_b32_e32 v4, s28, v1
	v_mov_b32_e32 v5, 0
	s_add_i32 s29, s28, 64
	v_lshl_add_u64 v[4:5], v[4:5], 4, s[6:7]
	v_or_b32_e32 v6, s29, v1
	v_mov_b32_e32 v7, 0
	s_addk_i32 s28, 0x80
	v_lshl_add_u64 v[6:7], v[6:7], 4, s[6:7]
	s_lshl_b32 s24, s5, 5
	v_and_or_b32 v8, v0, 31, s24
	v_mov_b32_e32 v9, 0
	v_lshl_add_u64 v[8:9], v[8:9], 2, s[44:45]
	global_load_dword v126, v[8:9], off
	global_load_dwordx4 v[72:75], v[4:5], off
	global_load_dwordx4 v[76:79], v[6:7], off
	v_or_b32_e32 v4, s28, v1
	v_mov_b32_e32 v5, 0
	v_lshl_add_u64 v[4:5], v[4:5], 4, s[6:7]
	global_load_dwordx4 v[80:83], v[4:5], off
	v_lshlrev_b32_e32 v88, 4, v0
	v_mov_b32_e32 v89, v18
	s_mov_b32 m0, s48
	s_nop 0
	global_load_lds_dwordx4 v88, s[62:63]
	s_add_u32 s54, s62, 0x2000
	s_addc_u32 s55, s63, 0
	s_add_u32 m0, s48, 0x2000
	s_nop 0
	global_load_lds_dwordx4 v88, s[54:55]
	s_add_u32 s54, s62, 0x4000
	s_addc_u32 s55, s63, 0
	s_add_u32 m0, s48, 0x4000
	s_nop 0
	global_load_lds_dwordx4 v88, s[54:55]
	s_add_u32 s54, s62, 0x6000
	s_addc_u32 s55, s63, 0
	s_add_u32 m0, s48, 0x6000
	s_nop 0
	global_load_lds_dwordx4 v88, s[54:55]
	s_lshl_b32 s24, s5, 5
	v_cmp_lt_u32_e32 vcc, 31, v1
	s_and_saveexec_b64 s[22:23], vcc
	s_cbranch_execz .LBB3_5
	s_mov_b64 s[6:7], s[44:45]
	s_mov_b64 s[26:27], s[46:47]
	s_lshl_b32 s25, s4, 6
	s_waitcnt lgkmcnt(0)
	s_load_dwordx16 s[4:19], s[26:27], s25 offset:0x0
	s_waitcnt lgkmcnt(0)
	v_max_f32_e64 v5, s4, s4
	v_mov_b32_e32 v6, s6
	v_max_f32_e32 v5, 0, v5
	v_mov_b32_e32 v7, s8
	v_min3_f32 v5, -v5, -s5, -v6
	v_mov_b32_e32 v8, s10
	v_min3_f32 v5, v5, -s7, -v7
	v_mov_b32_e32 v9, s12
	v_min3_f32 v5, v5, -s9, -v8
	v_mov_b32_e32 v10, s14
	v_min3_f32 v5, v5, -s11, -v9
	v_mov_b32_e32 v11, s16
	v_min3_f32 v5, v5, -s13, -v10
	v_mov_b32_e32 v12, s18
	v_min3_f32 v5, v5, -s15, -v11
	v_max_f32_e64 v13, -s19, -s19
	v_min3_f32 v5, v5, -s17, -v12
	v_min_f32_e32 v5, v5, v13
	s_mov_b32 s4, 0xffff
	s_waitcnt vmcnt(4)
	v_fma_mixlo_f16 v4, v126, v5, 0
	v_bfi_b32 v80, s4, v4, v80
.LBB3_5:
	s_or_b64 exec, exec, s[22:23]
	s_mov_b64 s[4:5], 0x10000
	s_mov_b64 s[4:5], 0x12000
	s_mov_b64 s[4:5], 0x14000
	s_mov_b64 s[4:5], 0x16000
	s_mov_b64 s[4:5], 0x18000
	s_mov_b64 s[4:5], 0x1a000
	s_mov_b64 s[4:5], 0x1c000
	s_mov_b64 s[4:5], 0x1e000
	v_lshlrev_b32_e32 v89, 4, v1
	s_mov_b64 s[6:7], 0
	s_mov_b64 s[4:5], -1
	v_mov_b32_e32 v19, v18
	v_mov_b32_e32 v20, v18
	v_mov_b32_e32 v21, v18
	v_mov_b32_e32 v84, v18
	v_mov_b32_e32 v85, v18
	v_mov_b32_e32 v86, v18
	v_mov_b32_e32 v87, v18
	s_waitcnt vmcnt(0)
	s_waitcnt lgkmcnt(0)
	s_barrier
	s_branch .LBB3_7
.LBB3_6:
	ds_read_b128 v[2:5], v89 offset:32768
	ds_read_b128 v[22:25], v89 offset:33792
	s_xor_b64 s[8:9], s[4:5], -1
	s_mov_b64 s[6:7], -1
	s_mov_b64 s[4:5], 0
	s_waitcnt lgkmcnt(1)
	v_mfma_f32_32x32x16_f16 v[2:17], v[2:5], v[72:75], 0
	s_and_b64 vcc, exec, s[8:9]
	s_waitcnt lgkmcnt(0)
	v_mfma_f32_32x32x16_f16 v[2:17], v[22:25], v[76:79], v[2:17]
	ds_read_b128 v[22:25], v89 offset:36864
	ds_read_b128 v[106:109], v89 offset:37888
	ds_read_b128 v[110:113], v89 offset:34816
	ds_read_b128 v[114:117], v89 offset:38912
	ds_read_b128 v[118:121], v89 offset:35840
	s_waitcnt lgkmcnt(4)
	v_mfma_f32_32x32x16_f16 v[24:39], v[22:25], v[72:75], 0
	s_waitcnt lgkmcnt(3)
	v_mfma_f32_32x32x16_f16 v[24:39], v[106:109], v[76:79], v[24:39]
	s_waitcnt lgkmcnt(2)
	v_mfma_f32_32x32x16_f16 v[2:17], v[110:113], v[80:83], v[2:17]
	s_waitcnt lgkmcnt(1)
	v_mfma_f32_32x32x16_f16 v[24:39], v[114:117], v[80:83], v[24:39]
	s_nop 9
	v_exp_f32_e32 v2, v2
	v_exp_f32_e32 v22, v3
	v_exp_f32_e32 v3, v4
	v_exp_f32_e32 v23, v5
	v_exp_f32_e32 v4, v6
	v_exp_f32_e32 v6, v7
	v_exp_f32_e32 v5, v8
	v_exp_f32_e32 v7, v9
	v_exp_f32_e32 v10, v10
	v_exp_f32_e32 v11, v11
	v_exp_f32_e32 v12, v12
	v_exp_f32_e32 v13, v13
	v_exp_f32_e32 v8, v14
	v_exp_f32_e32 v14, v15
	v_exp_f32_e32 v9, v16
	v_exp_f32_e32 v15, v17
	v_cvt_pk_bf16_f32 v5, v5, v7
	v_cvt_pk_bf16_f32 v4, v4, v6
	v_cvt_pk_bf16_f32 v3, v3, v23
	v_cvt_pk_bf16_f32 v2, v2, v22
	v_cvt_pk_bf16_f32 v9, v9, v15
	v_cvt_pk_bf16_f32 v8, v8, v14
	v_cvt_pk_bf16_f32 v7, v12, v13
	v_cvt_pk_bf16_f32 v6, v10, v11
	s_nop 1
	v_permlane16_swap_b32_e32 v2, v6
	v_permlane16_swap_b32_e32 v3, v7
	v_permlane16_swap_b32_e32 v4, v8
	v_permlane16_swap_b32_e32 v5, v9
	v_exp_f32_e32 v114, v24
	v_exp_f32_e32 v22, v26
	v_exp_f32_e32 v23, v28
	v_exp_f32_e32 v24, v30
	s_waitcnt lgkmcnt(0)
	v_mfma_f32_16x16x32_bf16 v[6:9], v[118:121], v[6:9], v[18:21]
	ds_read_b128 v[10:13], v89 offset:39936
	ds_read_b128 v[14:17], v89 offset:40960
	ds_read_b128 v[106:109], v89 offset:41984
	ds_read_b128 v[110:113], v89 offset:43008
	v_exp_f32_e32 v18, v31
	v_exp_f32_e32 v19, v29
	v_exp_f32_e32 v20, v27
	v_mfma_f32_16x16x32_bf16 v[2:5], v[118:121], v[2:5], v[84:87]
	s_nop 2
	v_exp_f32_e32 v84, v25
	v_cvt_pk_bf16_f32 v87, v24, v18
	v_cvt_pk_bf16_f32 v86, v23, v19
	v_cvt_pk_bf16_f32 v85, v22, v20
	s_waitcnt lgkmcnt(2)
	v_mfma_f32_32x32x16_f16 v[16:31], v[14:17], v[72:75], 0
	v_exp_f32_e32 v14, v32
	v_exp_f32_e32 v15, v34
	v_exp_f32_e32 v32, v36
	v_exp_f32_e32 v34, v37
	v_exp_f32_e32 v36, v38
	v_exp_f32_e32 v37, v39
	v_exp_f32_e32 v38, v35
	s_waitcnt lgkmcnt(1)
	v_mfma_f32_32x32x16_f16 v[16:31], v[106:109], v[76:79], v[16:31]
	v_exp_f32_e32 v39, v33
	v_cvt_pk_bf16_f32 v84, v114, v84
	v_cvt_pk_bf16_f32 v35, v36, v37
	v_cvt_pk_bf16_f32 v34, v32, v34
	v_cvt_pk_bf16_f32 v33, v15, v38
	v_cvt_pk_bf16_f32 v32, v14, v39
	s_nop 1
	v_permlane16_swap_b32_e32 v84, v32
	v_permlane16_swap_b32_e32 v85, v33
	v_permlane16_swap_b32_e32 v86, v34
	v_permlane16_swap_b32_e32 v87, v35
	ds_read_b128 v[36:39], v89 offset:44032
	s_nop 0
	v_mfma_f32_16x16x32_bf16 v[84:87], v[10:13], v[84:87], v[2:5]
	s_nop 2
	ds_read_b128 v[2:5], v89 offset:45056
	s_waitcnt lgkmcnt(2)
	v_mfma_f32_32x32x16_f16 v[16:31], v[110:113], v[80:83], v[16:31]
	v_mfma_f32_16x16x32_bf16 v[106:109], v[10:13], v[32:35], v[6:9]
	s_nop 10
	v_exp_f32_e32 v114, v16
	v_exp_f32_e32 v118, v17
	v_exp_f32_e32 v18, v18
	s_waitcnt lgkmcnt(0)
	v_mfma_f32_32x32x16_f16 v[2:17], v[2:5], v[72:75], 0
	v_exp_f32_e32 v20, v20
	v_exp_f32_e32 v21, v21
	v_exp_f32_e32 v19, v19
	ds_read_b128 v[32:35], v89 offset:46080
	ds_read_b128 v[110:113], v89 offset:47104
	v_cvt_pk_bf16_f32 v114, v114, v118
	v_cvt_pk_bf16_f32 v116, v20, v21
	v_cvt_pk_bf16_f32 v115, v18, v19
	ds_read_b128 v[118:121], v89 offset:48128
	ds_read_b128 v[18:21], v89 offset:49152
	v_exp_f32_e32 v22, v22
	v_exp_f32_e32 v23, v23
	s_waitcnt lgkmcnt(3)
	v_mfma_f32_32x32x16_f16 v[2:17], v[32:35], v[76:79], v[2:17]
	v_exp_f32_e32 v29, v29
	v_exp_f32_e32 v27, v27
	v_cvt_pk_bf16_f32 v117, v22, v23
	v_exp_f32_e32 v22, v24
	v_exp_f32_e32 v23, v26
	v_exp_f32_e32 v24, v28
	v_exp_f32_e32 v26, v30
	v_exp_f32_e32 v28, v31
	v_exp_f32_e32 v25, v25
	ds_read_b128 v[122:125], v89 offset:50176
	s_waitcnt lgkmcnt(3)
	v_mfma_f32_32x32x16_f16 v[2:17], v[110:113], v[80:83], v[2:17]
	v_cvt_pk_bf16_f32 v113, v26, v28
	v_cvt_pk_bf16_f32 v112, v24, v29
	v_cvt_pk_bf16_f32 v111, v23, v27
	v_cvt_pk_bf16_f32 v110, v22, v25
	s_nop 1
	v_permlane16_swap_b32_e32 v114, v110
	v_permlane16_swap_b32_e32 v115, v111
	s_waitcnt lgkmcnt(1)
	v_mfma_f32_32x32x16_f16 v[18:33], v[18:21], v[72:75], 0
	v_permlane16_swap_b32_e32 v116, v112
	v_permlane16_swap_b32_e32 v117, v113
	v_exp_f32_e32 v2, v2
	v_exp_f32_e32 v4, v4
	v_exp_f32_e32 v5, v5
	v_mfma_f32_16x16x32_bf16 v[84:87], v[36:39], v[114:117], v[84:87]
	v_exp_f32_e32 v3, v3
	v_exp_f32_e32 v6, v6
	v_exp_f32_e32 v7, v7
	v_mfma_f32_16x16x32_bf16 v[34:37], v[36:39], v[110:113], v[106:109]
	ds_read_b128 v[110:113], v89 offset:52224
	v_exp_f32_e32 v8, v8
	v_exp_f32_e32 v9, v9
	ds_read_b128 v[106:109], v89 offset:51200
	s_waitcnt lgkmcnt(2)
	v_mfma_f32_32x32x16_f16 v[18:33], v[122:125], v[76:79], v[18:33]
	v_exp_f32_e32 v13, v13
	v_exp_f32_e32 v11, v11
	ds_read_b128 v[122:125], v89 offset:54272
	s_waitcnt lgkmcnt(1)
	v_mfma_f32_32x32x16_f16 v[18:33], v[106:109], v[80:83], v[18:33]
	v_cvt_pk_bf16_f32 v107, v4, v5
	v_cvt_pk_bf16_f32 v106, v2, v3
	ds_read_b128 v[2:5], v89 offset:53248
	v_cvt_pk_bf16_f32 v109, v8, v9
	v_cvt_pk_bf16_f32 v108, v6, v7
	v_exp_f32_e32 v6, v10
	v_exp_f32_e32 v7, v12
	v_exp_f32_e32 v8, v14
	v_exp_f32_e32 v9, v16
	v_exp_f32_e32 v10, v17
	v_exp_f32_e32 v12, v15
	v_cvt_pk_bf16_f32 v115, v7, v13
	v_cvt_pk_bf16_f32 v114, v6, v11
	v_cvt_pk_bf16_f32 v117, v9, v10
	v_cvt_pk_bf16_f32 v116, v8, v12
	s_waitcnt lgkmcnt(0)
	v_mfma_f32_32x32x16_f16 v[2:17], v[2:5], v[72:75], 0
	v_permlane16_swap_b32_e32 v106, v114
	v_permlane16_swap_b32_e32 v107, v115
	v_permlane16_swap_b32_e32 v108, v116
	v_permlane16_swap_b32_e32 v109, v117
	v_mfma_f32_32x32x16_f16 v[2:17], v[122:125], v[76:79], v[2:17]
	v_exp_f32_e32 v18, v18
	v_exp_f32_e32 v20, v20
	v_exp_f32_e32 v21, v21
	v_exp_f32_e32 v19, v19
	v_exp_f32_e32 v22, v22
	v_exp_f32_e32 v24, v24
	v_exp_f32_e32 v25, v25
	v_mfma_f32_16x16x32_bf16 v[84:87], v[118:121], v[106:109], v[84:87]
	v_exp_f32_e32 v23, v23
	v_exp_f32_e32 v29, v29
	v_exp_f32_e32 v27, v27
	v_mfma_f32_16x16x32_bf16 v[34:37], v[118:121], v[114:117], v[34:37]
	ds_read_b128 v[106:109], v89 offset:55296
	ds_read_b128 v[114:117], v89 offset:56320
	ds_read_b128 v[122:125], v89 offset:58368
	s_waitcnt lgkmcnt(2)
	v_mfma_f32_32x32x16_f16 v[2:17], v[106:109], v[80:83], v[2:17]
	v_cvt_pk_bf16_f32 v107, v20, v21
	v_cvt_pk_bf16_f32 v106, v18, v19
	ds_read_b128 v[18:21], v89 offset:57344
	v_cvt_pk_bf16_f32 v109, v24, v25
	v_cvt_pk_bf16_f32 v108, v22, v23
	v_exp_f32_e32 v22, v26
	v_exp_f32_e32 v23, v28
	v_exp_f32_e32 v24, v30
	v_exp_f32_e32 v25, v32
	v_exp_f32_e32 v26, v33
	v_exp_f32_e32 v28, v31
	v_cvt_pk_bf16_f32 v119, v23, v29
	v_cvt_pk_bf16_f32 v118, v22, v27
	v_cvt_pk_bf16_f32 v121, v25, v26
	v_cvt_pk_bf16_f32 v120, v24, v28
	s_waitcnt lgkmcnt(0)
	v_mfma_f32_32x32x16_f16 v[18:33], v[18:21], v[72:75], 0
	v_permlane16_swap_b32_e32 v106, v118
	v_permlane16_swap_b32_e32 v107, v119
	v_permlane16_swap_b32_e32 v108, v120
	v_permlane16_swap_b32_e32 v109, v121
	v_mfma_f32_32x32x16_f16 v[18:33], v[122:125], v[76:79], v[18:33]
	v_exp_f32_e32 v2, v2
	v_exp_f32_e32 v4, v4
	v_exp_f32_e32 v5, v5
	v_exp_f32_e32 v3, v3
	v_exp_f32_e32 v6, v6
	v_exp_f32_e32 v8, v8
	v_exp_f32_e32 v9, v9
	v_mfma_f32_16x16x32_bf16 v[84:87], v[110:113], v[106:109], v[84:87]
	v_exp_f32_e32 v7, v7
	v_exp_f32_e32 v13, v13
	v_exp_f32_e32 v11, v11
	v_mfma_f32_16x16x32_bf16 v[34:37], v[110:113], v[118:121], v[34:37]
	ds_read_b128 v[106:109], v89 offset:59392
	ds_read_b128 v[110:113], v89 offset:60416
	ds_read_b128 v[122:125], v89 offset:62464
	s_waitcnt lgkmcnt(2)
	v_mfma_f32_32x32x16_f16 v[18:33], v[106:109], v[80:83], v[18:33]
	v_cvt_pk_bf16_f32 v107, v4, v5
	v_cvt_pk_bf16_f32 v106, v2, v3
	ds_read_b128 v[2:5], v89 offset:61440
	v_cvt_pk_bf16_f32 v109, v8, v9
	v_cvt_pk_bf16_f32 v108, v6, v7
	v_exp_f32_e32 v6, v10
	v_exp_f32_e32 v7, v12
	v_exp_f32_e32 v8, v14
	v_exp_f32_e32 v9, v16
	v_exp_f32_e32 v10, v17
	v_exp_f32_e32 v12, v15
	v_cvt_pk_bf16_f32 v119, v7, v13
	v_cvt_pk_bf16_f32 v118, v6, v11
	v_cvt_pk_bf16_f32 v121, v9, v10
	v_cvt_pk_bf16_f32 v120, v8, v12
	s_waitcnt lgkmcnt(0)
	v_mfma_f32_32x32x16_f16 v[2:17], v[2:5], v[72:75], 0
	v_permlane16_swap_b32_e32 v106, v118
	v_permlane16_swap_b32_e32 v107, v119
	v_permlane16_swap_b32_e32 v108, v120
	v_permlane16_swap_b32_e32 v109, v121
	v_mfma_f32_32x32x16_f16 v[2:17], v[122:125], v[76:79], v[2:17]
	v_exp_f32_e32 v38, v20
	v_exp_f32_e32 v20, v22
	v_exp_f32_e32 v22, v24
	v_exp_f32_e32 v24, v25
	v_exp_f32_e32 v25, v21
	v_exp_f32_e32 v23, v23
	v_exp_f32_e32 v39, v19
	v_mfma_f32_16x16x32_bf16 v[84:87], v[114:117], v[106:109], v[84:87]
	v_cvt_pk_bf16_f32 v21, v22, v24
	v_cvt_pk_bf16_f32 v19, v38, v25
	v_exp_f32_e32 v22, v26
	v_mfma_f32_16x16x32_bf16 v[34:37], v[114:117], v[118:121], v[34:37]
	ds_read_b128 v[106:109], v89 offset:63488
	ds_read_b128 v[114:117], v89 offset:64512
	v_exp_f32_e32 v25, v32
	v_exp_f32_e32 v26, v33
	s_waitcnt lgkmcnt(1)
	v_mfma_f32_32x32x16_f16 v[2:17], v[106:109], v[80:83], v[2:17]
	v_exp_f32_e32 v18, v18
	v_cvt_pk_bf16_f32 v20, v20, v23
	v_exp_f32_e32 v23, v28
	v_exp_f32_e32 v24, v30
	v_exp_f32_e32 v28, v31
	v_exp_f32_e32 v29, v29
	v_exp_f32_e32 v27, v27
	v_cvt_pk_bf16_f32 v25, v25, v26
	s_nop 3
	v_exp_f32_e32 v26, v4
	v_exp_f32_e32 v4, v6
	v_exp_f32_e32 v6, v8
	v_exp_f32_e32 v8, v9
	v_exp_f32_e32 v7, v7
	v_exp_f32_e32 v9, v5
	v_cvt_pk_bf16_f32 v18, v18, v39
	v_cvt_pk_bf16_f32 v24, v24, v28
	v_cvt_pk_bf16_f32 v23, v23, v29
	v_cvt_pk_bf16_f32 v22, v22, v27
	v_exp_f32_e32 v2, v2
	v_exp_f32_e32 v27, v3
	v_cvt_pk_bf16_f32 v5, v6, v8
	v_cvt_pk_bf16_f32 v4, v4, v7
	v_cvt_pk_bf16_f32 v3, v26, v9
	v_exp_f32_e32 v6, v10
	v_exp_f32_e32 v7, v12
	v_exp_f32_e32 v8, v14
	v_exp_f32_e32 v9, v16
	v_exp_f32_e32 v10, v17
	v_exp_f32_e32 v12, v15
	v_exp_f32_e32 v13, v13
	v_exp_f32_e32 v11, v11
	v_permlane16_swap_b32_e32 v18, v22
	v_permlane16_swap_b32_e32 v19, v23
	v_permlane16_swap_b32_e32 v20, v24
	v_permlane16_swap_b32_e32 v21, v25
	v_cvt_pk_bf16_f32 v2, v2, v27
	s_nop 0
	v_mfma_f32_16x16x32_bf16 v[18:21], v[110:113], v[18:21], v[84:87]
	v_cvt_pk_bf16_f32 v9, v9, v10
	v_cvt_pk_bf16_f32 v8, v8, v12
	v_cvt_pk_bf16_f32 v7, v7, v13
	v_mfma_f32_16x16x32_bf16 v[22:25], v[110:113], v[22:25], v[34:37]
	v_cvt_pk_bf16_f32 v6, v6, v11
	s_nop 1
	v_permlane16_swap_b32_e32 v2, v6
	v_permlane16_swap_b32_e32 v3, v7
	v_permlane16_swap_b32_e32 v4, v8
	v_permlane16_swap_b32_e32 v5, v9
	s_waitcnt lgkmcnt(0)
	s_nop 0
	v_mfma_f32_16x16x32_bf16 v[84:87], v[114:117], v[2:5], v[18:21]
	s_waitcnt vmcnt(0)
	s_barrier
	v_mfma_f32_16x16x32_bf16 v[18:21], v[114:117], v[6:9], v[22:25]
	s_cbranch_vccnz .LBB3_13
.LBB3_7:
	s_and_b64 vcc, exec, s[4:5]
	s_add_u32 m0, s48, 0x8000
	s_nop 0
	global_load_lds_dwordx4 v88, s[50:51]
	s_add_u32 s54, s50, 0x2000
	s_addc_u32 s55, s51, 0
	s_add_u32 m0, s48, 0xa000
	s_nop 0
	global_load_lds_dwordx4 v88, s[54:55]
	s_add_u32 s54, s50, 0x4000
	s_addc_u32 s55, s51, 0
	s_add_u32 m0, s48, 0xc000
	s_nop 0
	global_load_lds_dwordx4 v88, s[54:55]
	s_add_u32 s54, s50, 0x6000
	s_addc_u32 s55, s51, 0
	s_add_u32 m0, s48, 0xe000
	s_nop 0
	global_load_lds_dwordx4 v88, s[54:55]
	s_add_u32 s50, s50, 0x10000
	s_addc_u32 s51, s51, 0
.LBB3_9:
	ds_read_b128 v[2:5], v89
	ds_read_b128 v[22:25], v89 offset:1024
	s_xor_b64 s[6:7], s[6:7], -1
	s_andn2_b64 vcc, exec, s[6:7]
	s_waitcnt lgkmcnt(1)
	v_mfma_f32_32x32x16_f16 v[2:17], v[2:5], v[72:75], 0
	s_waitcnt lgkmcnt(0)
	v_mfma_f32_32x32x16_f16 v[2:17], v[22:25], v[76:79], v[2:17]
	ds_read_b128 v[22:25], v89 offset:4096
	ds_read_b128 v[106:109], v89 offset:5120
	ds_read_b128 v[110:113], v89 offset:2048
	ds_read_b128 v[114:117], v89 offset:6144
	ds_read_b128 v[118:121], v89 offset:3072
	s_waitcnt lgkmcnt(4)
	v_mfma_f32_32x32x16_f16 v[24:39], v[22:25], v[72:75], 0
	s_waitcnt lgkmcnt(3)
	v_mfma_f32_32x32x16_f16 v[24:39], v[106:109], v[76:79], v[24:39]
	s_waitcnt lgkmcnt(2)
	v_mfma_f32_32x32x16_f16 v[2:17], v[110:113], v[80:83], v[2:17]
	s_waitcnt lgkmcnt(1)
	v_mfma_f32_32x32x16_f16 v[24:39], v[114:117], v[80:83], v[24:39]
	s_nop 9
	v_exp_f32_e32 v2, v2
	v_exp_f32_e32 v22, v3
	v_exp_f32_e32 v3, v4
	v_exp_f32_e32 v23, v5
	v_exp_f32_e32 v4, v6
	v_exp_f32_e32 v6, v7
	v_exp_f32_e32 v5, v8
	v_exp_f32_e32 v7, v9
	v_exp_f32_e32 v10, v10
	v_exp_f32_e32 v11, v11
	v_exp_f32_e32 v12, v12
	v_exp_f32_e32 v13, v13
	v_exp_f32_e32 v8, v14
	v_exp_f32_e32 v14, v15
	v_exp_f32_e32 v9, v16
	v_exp_f32_e32 v15, v17
	v_cvt_pk_bf16_f32 v5, v5, v7
	v_cvt_pk_bf16_f32 v4, v4, v6
	v_cvt_pk_bf16_f32 v3, v3, v23
	v_cvt_pk_bf16_f32 v2, v2, v22
	v_cvt_pk_bf16_f32 v9, v9, v15
	v_cvt_pk_bf16_f32 v8, v8, v14
	v_cvt_pk_bf16_f32 v7, v12, v13
	v_cvt_pk_bf16_f32 v6, v10, v11
	s_nop 1
	v_permlane16_swap_b32_e32 v2, v6
	v_permlane16_swap_b32_e32 v3, v7
	v_permlane16_swap_b32_e32 v4, v8
	v_permlane16_swap_b32_e32 v5, v9
	v_exp_f32_e32 v114, v24
	v_exp_f32_e32 v22, v26
	v_exp_f32_e32 v23, v28
	v_exp_f32_e32 v24, v30
	s_waitcnt lgkmcnt(0)
	v_mfma_f32_16x16x32_bf16 v[6:9], v[118:121], v[6:9], v[18:21]
	ds_read_b128 v[10:13], v89 offset:7168
	ds_read_b128 v[14:17], v89 offset:8192
	ds_read_b128 v[106:109], v89 offset:9216
	ds_read_b128 v[110:113], v89 offset:10240
	v_exp_f32_e32 v18, v31
	v_exp_f32_e32 v19, v29
	v_exp_f32_e32 v20, v27
	v_mfma_f32_16x16x32_bf16 v[2:5], v[118:121], v[2:5], v[84:87]
	s_nop 2
	v_exp_f32_e32 v84, v25
	v_cvt_pk_bf16_f32 v87, v24, v18
	v_cvt_pk_bf16_f32 v86, v23, v19
	v_cvt_pk_bf16_f32 v85, v22, v20
	s_waitcnt lgkmcnt(2)
	v_mfma_f32_32x32x16_f16 v[16:31], v[14:17], v[72:75], 0
	v_exp_f32_e32 v14, v32
	v_exp_f32_e32 v15, v34
	v_exp_f32_e32 v32, v36
	v_exp_f32_e32 v34, v37
	v_exp_f32_e32 v36, v38
	v_exp_f32_e32 v37, v39
	v_exp_f32_e32 v38, v35
	s_waitcnt lgkmcnt(1)
	v_mfma_f32_32x32x16_f16 v[16:31], v[106:109], v[76:79], v[16:31]
	v_exp_f32_e32 v39, v33
	v_cvt_pk_bf16_f32 v84, v114, v84
	v_cvt_pk_bf16_f32 v35, v36, v37
	v_cvt_pk_bf16_f32 v34, v32, v34
	v_cvt_pk_bf16_f32 v33, v15, v38
	v_cvt_pk_bf16_f32 v32, v14, v39
	s_nop 1
	v_permlane16_swap_b32_e32 v84, v32
	v_permlane16_swap_b32_e32 v85, v33
	v_permlane16_swap_b32_e32 v86, v34
	v_permlane16_swap_b32_e32 v87, v35
	ds_read_b128 v[36:39], v89 offset:11264
	s_nop 0
	v_mfma_f32_16x16x32_bf16 v[84:87], v[10:13], v[84:87], v[2:5]
	s_nop 2
	ds_read_b128 v[2:5], v89 offset:12288
	s_waitcnt lgkmcnt(2)
	v_mfma_f32_32x32x16_f16 v[16:31], v[110:113], v[80:83], v[16:31]
	v_mfma_f32_16x16x32_bf16 v[106:109], v[10:13], v[32:35], v[6:9]
	s_nop 10
	v_exp_f32_e32 v114, v16
	v_exp_f32_e32 v118, v17
	v_exp_f32_e32 v18, v18
	s_waitcnt lgkmcnt(0)
	v_mfma_f32_32x32x16_f16 v[2:17], v[2:5], v[72:75], 0
	v_exp_f32_e32 v20, v20
	v_exp_f32_e32 v21, v21
	v_exp_f32_e32 v19, v19
	ds_read_b128 v[32:35], v89 offset:13312
	ds_read_b128 v[110:113], v89 offset:14336
	v_cvt_pk_bf16_f32 v114, v114, v118
	v_cvt_pk_bf16_f32 v116, v20, v21
	v_cvt_pk_bf16_f32 v115, v18, v19
	ds_read_b128 v[118:121], v89 offset:15360
	ds_read_b128 v[18:21], v89 offset:16384
	v_exp_f32_e32 v22, v22
	v_exp_f32_e32 v23, v23
	s_waitcnt lgkmcnt(3)
	v_mfma_f32_32x32x16_f16 v[2:17], v[32:35], v[76:79], v[2:17]
	v_exp_f32_e32 v29, v29
	v_exp_f32_e32 v27, v27
	v_cvt_pk_bf16_f32 v117, v22, v23
	v_exp_f32_e32 v22, v24
	v_exp_f32_e32 v23, v26
	v_exp_f32_e32 v24, v28
	v_exp_f32_e32 v26, v30
	v_exp_f32_e32 v28, v31
	v_exp_f32_e32 v25, v25
	ds_read_b128 v[122:125], v89 offset:17408
	s_waitcnt lgkmcnt(3)
	v_mfma_f32_32x32x16_f16 v[2:17], v[110:113], v[80:83], v[2:17]
	v_cvt_pk_bf16_f32 v113, v26, v28
	v_cvt_pk_bf16_f32 v112, v24, v29
	v_cvt_pk_bf16_f32 v111, v23, v27
	v_cvt_pk_bf16_f32 v110, v22, v25
	s_nop 1
	v_permlane16_swap_b32_e32 v114, v110
	v_permlane16_swap_b32_e32 v115, v111
	s_waitcnt lgkmcnt(1)
	v_mfma_f32_32x32x16_f16 v[18:33], v[18:21], v[72:75], 0
	v_permlane16_swap_b32_e32 v116, v112
	v_permlane16_swap_b32_e32 v117, v113
	v_exp_f32_e32 v2, v2
	v_exp_f32_e32 v4, v4
	v_exp_f32_e32 v5, v5
	v_mfma_f32_16x16x32_bf16 v[84:87], v[36:39], v[114:117], v[84:87]
	v_exp_f32_e32 v3, v3
	v_exp_f32_e32 v6, v6
	v_exp_f32_e32 v7, v7
	v_mfma_f32_16x16x32_bf16 v[34:37], v[36:39], v[110:113], v[106:109]
	ds_read_b128 v[110:113], v89 offset:19456
	v_exp_f32_e32 v8, v8
	v_exp_f32_e32 v9, v9
	ds_read_b128 v[106:109], v89 offset:18432
	s_waitcnt lgkmcnt(2)
	v_mfma_f32_32x32x16_f16 v[18:33], v[122:125], v[76:79], v[18:33]
	v_exp_f32_e32 v13, v13
	v_exp_f32_e32 v11, v11
	ds_read_b128 v[122:125], v89 offset:21504
	s_waitcnt lgkmcnt(1)
	v_mfma_f32_32x32x16_f16 v[18:33], v[106:109], v[80:83], v[18:33]
	v_cvt_pk_bf16_f32 v107, v4, v5
	v_cvt_pk_bf16_f32 v106, v2, v3
	ds_read_b128 v[2:5], v89 offset:20480
	v_cvt_pk_bf16_f32 v109, v8, v9
	v_cvt_pk_bf16_f32 v108, v6, v7
	v_exp_f32_e32 v6, v10
	v_exp_f32_e32 v7, v12
	v_exp_f32_e32 v8, v14
	v_exp_f32_e32 v9, v16
	v_exp_f32_e32 v10, v17
	v_exp_f32_e32 v12, v15
	v_cvt_pk_bf16_f32 v115, v7, v13
	v_cvt_pk_bf16_f32 v114, v6, v11
	v_cvt_pk_bf16_f32 v117, v9, v10
	v_cvt_pk_bf16_f32 v116, v8, v12
	s_waitcnt lgkmcnt(0)
	v_mfma_f32_32x32x16_f16 v[2:17], v[2:5], v[72:75], 0
	v_permlane16_swap_b32_e32 v106, v114
	v_permlane16_swap_b32_e32 v107, v115
	v_permlane16_swap_b32_e32 v108, v116
	v_permlane16_swap_b32_e32 v109, v117
	v_mfma_f32_32x32x16_f16 v[2:17], v[122:125], v[76:79], v[2:17]
	v_exp_f32_e32 v18, v18
	v_exp_f32_e32 v20, v20
	v_exp_f32_e32 v21, v21
	v_exp_f32_e32 v19, v19
	v_exp_f32_e32 v22, v22
	v_exp_f32_e32 v24, v24
	v_exp_f32_e32 v25, v25
	v_mfma_f32_16x16x32_bf16 v[84:87], v[118:121], v[106:109], v[84:87]
	v_exp_f32_e32 v23, v23
	v_exp_f32_e32 v29, v29
	v_exp_f32_e32 v27, v27
	v_mfma_f32_16x16x32_bf16 v[34:37], v[118:121], v[114:117], v[34:37]
	ds_read_b128 v[106:109], v89 offset:22528
	ds_read_b128 v[114:117], v89 offset:23552
	ds_read_b128 v[122:125], v89 offset:25600
	s_waitcnt lgkmcnt(2)
	v_mfma_f32_32x32x16_f16 v[2:17], v[106:109], v[80:83], v[2:17]
	v_cvt_pk_bf16_f32 v107, v20, v21
	v_cvt_pk_bf16_f32 v106, v18, v19
	ds_read_b128 v[18:21], v89 offset:24576
	v_cvt_pk_bf16_f32 v109, v24, v25
	v_cvt_pk_bf16_f32 v108, v22, v23
	v_exp_f32_e32 v22, v26
	v_exp_f32_e32 v23, v28
	v_exp_f32_e32 v24, v30
	v_exp_f32_e32 v25, v32
	v_exp_f32_e32 v26, v33
	v_exp_f32_e32 v28, v31
	v_cvt_pk_bf16_f32 v119, v23, v29
	v_cvt_pk_bf16_f32 v118, v22, v27
	v_cvt_pk_bf16_f32 v121, v25, v26
	v_cvt_pk_bf16_f32 v120, v24, v28
	s_waitcnt lgkmcnt(0)
	v_mfma_f32_32x32x16_f16 v[18:33], v[18:21], v[72:75], 0
	v_permlane16_swap_b32_e32 v106, v118
	v_permlane16_swap_b32_e32 v107, v119
	v_permlane16_swap_b32_e32 v108, v120
	v_permlane16_swap_b32_e32 v109, v121
	v_mfma_f32_32x32x16_f16 v[18:33], v[122:125], v[76:79], v[18:33]
	v_exp_f32_e32 v2, v2
	v_exp_f32_e32 v4, v4
	v_exp_f32_e32 v5, v5
	v_exp_f32_e32 v3, v3
	v_exp_f32_e32 v6, v6
	v_exp_f32_e32 v8, v8
	v_exp_f32_e32 v9, v9
	v_mfma_f32_16x16x32_bf16 v[84:87], v[110:113], v[106:109], v[84:87]
	v_exp_f32_e32 v7, v7
	v_exp_f32_e32 v13, v13
	v_exp_f32_e32 v11, v11
	v_mfma_f32_16x16x32_bf16 v[34:37], v[110:113], v[118:121], v[34:37]
	ds_read_b128 v[106:109], v89 offset:26624
	ds_read_b128 v[110:113], v89 offset:27648
	ds_read_b128 v[122:125], v89 offset:29696
	s_waitcnt lgkmcnt(2)
	v_mfma_f32_32x32x16_f16 v[18:33], v[106:109], v[80:83], v[18:33]
	v_cvt_pk_bf16_f32 v107, v4, v5
	v_cvt_pk_bf16_f32 v106, v2, v3
	ds_read_b128 v[2:5], v89 offset:28672
	v_cvt_pk_bf16_f32 v109, v8, v9
	v_cvt_pk_bf16_f32 v108, v6, v7
	v_exp_f32_e32 v6, v10
	v_exp_f32_e32 v7, v12
	v_exp_f32_e32 v8, v14
	v_exp_f32_e32 v9, v16
	v_exp_f32_e32 v10, v17
	v_exp_f32_e32 v12, v15
	v_cvt_pk_bf16_f32 v119, v7, v13
	v_cvt_pk_bf16_f32 v118, v6, v11
	v_cvt_pk_bf16_f32 v121, v9, v10
	v_cvt_pk_bf16_f32 v120, v8, v12
	s_waitcnt lgkmcnt(0)
	v_mfma_f32_32x32x16_f16 v[2:17], v[2:5], v[72:75], 0
	v_permlane16_swap_b32_e32 v106, v118
	v_permlane16_swap_b32_e32 v107, v119
	v_permlane16_swap_b32_e32 v108, v120
	v_permlane16_swap_b32_e32 v109, v121
	v_mfma_f32_32x32x16_f16 v[2:17], v[122:125], v[76:79], v[2:17]
	v_exp_f32_e32 v38, v20
	v_exp_f32_e32 v20, v22
	v_exp_f32_e32 v22, v24
	v_exp_f32_e32 v24, v25
	v_exp_f32_e32 v25, v21
	v_exp_f32_e32 v23, v23
	v_exp_f32_e32 v39, v19
	v_mfma_f32_16x16x32_bf16 v[84:87], v[114:117], v[106:109], v[84:87]
	v_cvt_pk_bf16_f32 v21, v22, v24
	v_cvt_pk_bf16_f32 v19, v38, v25
	v_exp_f32_e32 v22, v26
	v_mfma_f32_16x16x32_bf16 v[34:37], v[114:117], v[118:121], v[34:37]
	ds_read_b128 v[106:109], v89 offset:30720
	ds_read_b128 v[114:117], v89 offset:31744
	v_exp_f32_e32 v25, v32
	v_exp_f32_e32 v26, v33
	s_waitcnt lgkmcnt(1)
	v_mfma_f32_32x32x16_f16 v[2:17], v[106:109], v[80:83], v[2:17]
	v_exp_f32_e32 v18, v18
	v_cvt_pk_bf16_f32 v20, v20, v23
	v_exp_f32_e32 v23, v28
	v_exp_f32_e32 v24, v30
	v_exp_f32_e32 v28, v31
	v_exp_f32_e32 v29, v29
	v_exp_f32_e32 v27, v27
	v_cvt_pk_bf16_f32 v25, v25, v26
	s_nop 3
	v_exp_f32_e32 v26, v4
	v_exp_f32_e32 v4, v6
	v_exp_f32_e32 v6, v8
	v_exp_f32_e32 v8, v9
	v_exp_f32_e32 v7, v7
	v_exp_f32_e32 v9, v5
	v_cvt_pk_bf16_f32 v18, v18, v39
	v_cvt_pk_bf16_f32 v24, v24, v28
	v_cvt_pk_bf16_f32 v23, v23, v29
	v_cvt_pk_bf16_f32 v22, v22, v27
	v_exp_f32_e32 v2, v2
	v_exp_f32_e32 v27, v3
	v_cvt_pk_bf16_f32 v5, v6, v8
	v_cvt_pk_bf16_f32 v4, v4, v7
	v_cvt_pk_bf16_f32 v3, v26, v9
	v_exp_f32_e32 v6, v10
	v_exp_f32_e32 v7, v12
	v_exp_f32_e32 v8, v14
	v_exp_f32_e32 v9, v16
	v_exp_f32_e32 v10, v17
	v_exp_f32_e32 v12, v15
	v_exp_f32_e32 v13, v13
	v_exp_f32_e32 v11, v11
	v_permlane16_swap_b32_e32 v18, v22
	v_permlane16_swap_b32_e32 v19, v23
	v_permlane16_swap_b32_e32 v20, v24
	v_permlane16_swap_b32_e32 v21, v25
	v_cvt_pk_bf16_f32 v2, v2, v27
	s_nop 0
	v_mfma_f32_16x16x32_bf16 v[18:21], v[110:113], v[18:21], v[84:87]
	v_cvt_pk_bf16_f32 v9, v9, v10
	v_cvt_pk_bf16_f32 v8, v8, v12
	v_cvt_pk_bf16_f32 v7, v7, v13
	v_mfma_f32_16x16x32_bf16 v[22:25], v[110:113], v[22:25], v[34:37]
	v_cvt_pk_bf16_f32 v6, v6, v11
	s_nop 1
	v_permlane16_swap_b32_e32 v2, v6
	v_permlane16_swap_b32_e32 v3, v7
	v_permlane16_swap_b32_e32 v4, v8
	v_permlane16_swap_b32_e32 v5, v9
	s_waitcnt lgkmcnt(0)
	s_nop 0
	v_mfma_f32_16x16x32_bf16 v[84:87], v[114:117], v[2:5], v[18:21]
	s_waitcnt vmcnt(0)
	s_barrier
	v_mfma_f32_16x16x32_bf16 v[18:21], v[114:117], v[6:9], v[22:25]
	s_cbranch_vccnz .LBB3_11
	s_mov_b32 m0, s48
	s_nop 0
	global_load_lds_dwordx4 v88, s[52:53]
	s_add_u32 s54, s52, 0x2000
	s_addc_u32 s55, s53, 0
	s_add_u32 m0, s48, 0x2000
	s_nop 0
	global_load_lds_dwordx4 v88, s[54:55]
	s_add_u32 s54, s52, 0x4000
	s_addc_u32 s55, s53, 0
	s_add_u32 m0, s48, 0x4000
	s_nop 0
	global_load_lds_dwordx4 v88, s[54:55]
	s_add_u32 s54, s52, 0x6000
	s_addc_u32 s55, s53, 0
	s_add_u32 m0, s48, 0x6000
	s_nop 0
	global_load_lds_dwordx4 v88, s[54:55]
.LBB3_11:
	s_andn2_b64 vcc, exec, s[4:5]
	s_cbranch_vccnz .LBB3_6
	s_branch .LBB3_6
